# SGU unit: epilogue bias + u loads issued before the MFMA part (on top of v7 stack)
# baseline (speedup 1.0000x reference)
; #define LAS __attribute__((address_space(3)))
; __device__ __forceinline__ void sgu_unit(const Params& p, int l, int un, LAS unsigned char* lds) {
;     ...
;     __syncthreads();
;     { const int fr = lane & 15, fq = lane >> 4; f32x4 acc[8];
; #pragma unroll
;       for (int nb = 0; nb < 8; ++nb) acc[nb] = (f32x4){0.f, 0.f, 0.f, 0.f};
; #pragma unroll
;       for (int ks = 0; ks < 4; ++ks) { const bf16x8 af = *(const LAS bf16x8*)(Wl + (wave * 16 + fr) * 136 + ks * 32 + fq * 8);
; #pragma unroll
;           for (int nb = 0; nb < 8; ++nb) { const bf16x8 bfr = *(const LAS bf16x8*)(Vl + (nb * 16 + fr) * 136 + ks * 32 + fq * 8);
;               acc[nb] = __builtin_amdgcn_mfma_f32_16x16x32_bf16(bfr, af, acc[nb], 0, 0, 0); } }
;       const int pp = wave * 16 + fr; const float bias = p.in[I_SGUB][((size_t)l * 4 + h) * 128 + pp]; const bf16_t* pr = P + (size_t)(row0 + pp) * INP + C_SGU_U + h * 128;
;       u32x2 uq[8];
; #pragma unroll
;       for (int nb = 0; nb < 8; ++nb) uq[nb] = *(const u32x2*)(pr + nb * 16 + 4 * fq);
.LBB0_1292:
	s_or_b64 exec, exec, s[0:1]
	v_and_b32_e32 v7, 15, v64
	v_or_b32_e32 v36, v65, v7
	v_lshl_add_u32 v6, v66, 4, 0
	v_mad_u64_u32 v[34:35], s[2:3], v36, s13, v[6:7]
	v_mad_u32_u24 v35, v7, s13, v6
	v_bfe_u32 v170, v0, 4, 2
	v_bfe_u32 v171, v0, 3, 1
	v_xor_b32_e32 v172, v170, v171
	v_sub_u32_e32 v172, v172, v170
	v_lshl_add_u32 v172, v172, 4, v35
	v_xor_b32_e32 v173, 2, v170
	v_xor_b32_e32 v173, v173, v171
	v_sub_u32_e32 v173, v173, v170
	v_lshl_add_u32 v173, v173, 4, v35
	v_ashrrev_i32_e32 v139, 31, v36
	v_mov_b32_e32 v138, v36
	s_lshl_b64 s[0:1], s[40:41], 2
	v_readlane_b32 s2, v251, 24
	v_readlane_b32 s3, v251, 25
	s_add_u32 s0, s2, s0
	s_addc_u32 s1, s3, s1
	v_lshl_add_u64 v[140:141], v[138:139], 2, s[0:1]
	global_load_dword v136, v[140:141], off
	s_movk_i32 s0, 0x1e00
	v_add_u32_e32 v137, s12, v36
	v_mov_b64_e32 v[140:141], s[38:39]
	v_mad_i64_i32 v[140:141], s[0:1], v137, s0, v[140:141]
	v_readlane_b32 s0, v253, 39
	s_lshl_b32 s0, s0, 1
	s_mov_b32 s1, s5
	v_lshlrev_b32_e32 v142, 3, v66
	v_mov_b32_e32 v143, 0
	v_lshl_add_u64 v[140:141], v[140:141], 0, s[0:1]
	v_lshl_add_u64 v[140:141], v[140:141], 0, v[142:143]
	global_load_dwordx2 v[120:121], v[140:141], off
	global_load_dwordx2 v[122:123], v[140:141], off offset:32
	global_load_dwordx2 v[124:125], v[140:141], off offset:64
	global_load_dwordx2 v[126:127], v[140:141], off offset:96
	global_load_dwordx2 v[128:129], v[140:141], off offset:128
	global_load_dwordx2 v[130:131], v[140:141], off offset:160
	global_load_dwordx2 v[132:133], v[140:141], off offset:192
	global_load_dwordx2 v[134:135], v[140:141], off offset:224
	s_waitcnt lgkmcnt(0)
	s_barrier
	ds_read_b128 v[2:5], v34
	ds_read_b128 v[6:9], v172 offset:34816
	ds_read_b128 v[10:13], v173 offset:39168
	ds_read_b128 v[14:17], v172 offset:43584
	ds_read_b128 v[18:21], v173 offset:47936
	ds_read_b128 v[22:25], v172 offset:52352
	ds_read_b128 v[26:29], v173 offset:56704
	ds_read_b128 v[30:33], v172 offset:61120
	ds_read_b128 v[38:41], v173 offset:65472
	s_waitcnt lgkmcnt(7)
	v_mfma_f32_16x16x32_bf16 v[6:9], v[6:9], v[2:5], 0
	s_lshl_b64 s[0:1], s[40:41], 2
	v_readlane_b32 s40, v251, 16
	v_readlane_b32 s41, v251, 17
	s_waitcnt lgkmcnt(6)
	v_mfma_f32_16x16x32_bf16 v[10:13], v[10:13], v[2:5], 0
	v_readlane_b32 s42, v251, 18
	v_readlane_b32 s43, v251, 19
	v_readlane_b32 s44, v251, 20
	s_waitcnt lgkmcnt(5)
	v_mfma_f32_16x16x32_bf16 v[14:17], v[14:17], v[2:5], 0
	v_readlane_b32 s45, v251, 21
	v_readlane_b32 s46, v251, 22
	v_readlane_b32 s47, v251, 23
	s_waitcnt lgkmcnt(4)
	v_mfma_f32_16x16x32_bf16 v[18:21], v[18:21], v[2:5], 0
	v_readlane_b32 s48, v251, 24
	v_readlane_b32 s49, v251, 25
	v_readlane_b32 s50, v251, 26
	s_waitcnt lgkmcnt(3)
	v_mfma_f32_16x16x32_bf16 v[22:25], v[22:25], v[2:5], 0
	v_readlane_b32 s51, v251, 27
	s_mov_b64 s[40:41], s[44:45]
	s_mov_b64 s[42:43], s[46:47]
	s_waitcnt lgkmcnt(2)
	v_mfma_f32_16x16x32_bf16 v[26:29], v[26:29], v[2:5], 0
	s_mov_b64 s[44:45], s[48:49]
	s_add_u32 s0, s44, s0
	s_addc_u32 s1, s45, s1
	s_waitcnt lgkmcnt(1)
	v_mfma_f32_16x16x32_bf16 v[30:33], v[30:33], v[2:5], 0
	v_ashrrev_i32_e32 v37, 31, v36
	v_lshlrev_b32_e32 v206, 3, v66
	v_readlane_b32 s52, v251, 28
	s_waitcnt lgkmcnt(0)
	v_mfma_f32_16x16x32_bf16 v[2:5], v[38:41], v[2:5], 0
	ds_read_b128 v[38:41], v34 offset:64
	ds_read_b128 v[42:45], v172 offset:34880
	v_readlane_b32 s53, v251, 29
	v_readlane_b32 s54, v251, 30
	s_waitcnt lgkmcnt(0)
	v_mfma_f32_16x16x32_bf16 v[6:9], v[42:45], v[38:41], v[6:9]
	ds_read_b128 v[42:45], v173 offset:39232
	v_readlane_b32 s55, v251, 31
	s_mov_b64 s[46:47], s[50:51]
	s_waitcnt lgkmcnt(0)
	v_mfma_f32_16x16x32_bf16 v[10:13], v[42:45], v[38:41], v[10:13]
	ds_read_b128 v[42:45], v172 offset:43520
	s_waitcnt lgkmcnt(0)
	v_mfma_f32_16x16x32_bf16 v[14:17], v[42:45], v[38:41], v[14:17]
	ds_read_b128 v[42:45], v173 offset:47872
	s_waitcnt lgkmcnt(0)
	v_mfma_f32_16x16x32_bf16 v[18:21], v[42:45], v[38:41], v[18:21]
	ds_read_b128 v[42:45], v172 offset:52416
	s_waitcnt lgkmcnt(0)
	v_mfma_f32_16x16x32_bf16 v[22:25], v[42:45], v[38:41], v[22:25]
	ds_read_b128 v[42:45], v173 offset:56768
	s_waitcnt lgkmcnt(0)
	v_mfma_f32_16x16x32_bf16 v[26:29], v[42:45], v[38:41], v[26:29]
	ds_read_b128 v[42:45], v172 offset:61056
	s_waitcnt lgkmcnt(0)
	v_mfma_f32_16x16x32_bf16 v[30:33], v[42:45], v[38:41], v[30:33]
	ds_read_b128 v[42:45], v173 offset:65408
	s_waitcnt lgkmcnt(0)
	v_mfma_f32_16x16x32_bf16 v[2:5], v[42:45], v[38:41], v[2:5]
	ds_read_b128 v[38:41], v34 offset:128
	ds_read_b128 v[42:45], v172 offset:34944
	s_waitcnt lgkmcnt(0)
	v_mfma_f32_16x16x32_bf16 v[6:9], v[42:45], v[38:41], v[6:9]
	ds_read_b128 v[42:45], v173 offset:39296
	s_waitcnt lgkmcnt(0)
	v_mfma_f32_16x16x32_bf16 v[10:13], v[42:45], v[38:41], v[10:13]
	ds_read_b128 v[42:45], v172 offset:43712
	s_waitcnt lgkmcnt(0)
	v_mfma_f32_16x16x32_bf16 v[14:17], v[42:45], v[38:41], v[14:17]
	ds_read_b128 v[42:45], v173 offset:48064
	s_waitcnt lgkmcnt(0)
	v_mfma_f32_16x16x32_bf16 v[18:21], v[42:45], v[38:41], v[18:21]
	ds_read_b128 v[42:45], v172 offset:52224
	s_waitcnt lgkmcnt(0)
	v_mfma_f32_16x16x32_bf16 v[42:45], v[42:45], v[38:41], v[22:25]
	s_nop 2
	ds_read_b128 v[22:25], v173 offset:56576
	s_waitcnt lgkmcnt(0)
	v_mfma_f32_16x16x32_bf16 v[46:49], v[22:25], v[38:41], v[26:29]
	ds_read_b128 v[22:25], v172 offset:60992
	s_waitcnt lgkmcnt(0)
	v_mfma_f32_16x16x32_bf16 v[50:53], v[22:25], v[38:41], v[30:33]
	ds_read_b128 v[22:25], v173 offset:65344
	s_waitcnt lgkmcnt(0)
	v_mfma_f32_16x16x32_bf16 v[2:5], v[22:25], v[38:41], v[2:5]
	ds_read_b128 v[38:41], v34 offset:192
	ds_read_b128 v[22:25], v172 offset:35008
	s_waitcnt lgkmcnt(0)
; #define LAS __attribute__((address_space(3)))
; __device__ __forceinline__ unsigned cvt_pk_bf16(float lo, float hi) { const f32x2 v = {lo, hi}; const bf16x2_t b = __builtin_convertvector(v, bf16x2_t); return __builtin_bit_cast(unsigned, b); }
; __device__ __forceinline__ float bflo(unsigned w) { return __uint_as_float(w << 16); }
; __device__ __forceinline__ float bfhi(unsigned w) { return __uint_as_float(w & 0xffff0000u); }
; __device__ __forceinline__ void sgu_unit(const Params& p, int l, int un, LAS unsigned char* lds) {
;     ...
;       for (int ks = 0; ks < 4; ++ks) { const bf16x8 af = *(const LAS bf16x8*)(Wl + (wave * 16 + fr) * 136 + ks * 32 + fq * 8);
; #pragma unroll
;           for (int nb = 0; nb < 8; ++nb) { const bf16x8 bfr = *(const LAS bf16x8*)(Vl + (nb * 16 + fr) * 136 + ks * 32 + fq * 8);
;               acc[nb] = __builtin_amdgcn_mfma_f32_16x16x32_bf16(bfr, af, acc[nb], 0, 0, 0); } }
;       const int pp = wave * 16 + fr; const float bias = p.in[I_SGUB][((size_t)l * 4 + h) * 128 + pp]; const bf16_t* pr = P + (size_t)(row0 + pp) * INP + C_SGU_U + h * 128;
;       u32x2 uq[8];
; #pragma unroll
;       for (int nb = 0; nb < 8; ++nb) uq[nb] = *(const u32x2*)(pr + nb * 16 + 4 * fq);
; #pragma unroll
;       for (int nb = 0; nb < 8; ++nb) { const int c = nb * 16 + 4 * fq; const u32x2 uv = uq[nb];
;           u32x2 w; w.x = cvt_pk_bf16(gelu_tanh(bflo(uv.x)) * (acc[nb][0] + bias), gelu_tanh(bfhi(uv.x)) * (acc[nb][1] + bias));
;           w.y = cvt_pk_bf16(gelu_tanh(bflo(uv.y)) * (acc[nb][2] + bias), gelu_tanh(bfhi(uv.y)) * (acc[nb][3] + bias));
;           *(u32x2*)(CAT + (size_t)(row0 + pp) * DM + h * 128 + c) = w; } }
	v_mfma_f32_16x16x32_bf16 v[30:33], v[22:25], v[38:41], v[6:9]
	s_nop 2
	ds_read_b128 v[6:9], v173 offset:39360
	s_waitcnt lgkmcnt(0)
	v_mfma_f32_16x16x32_bf16 v[26:29], v[6:9], v[38:41], v[10:13]
	ds_read_b128 v[6:9], v172 offset:43648
	s_waitcnt lgkmcnt(0)
	v_mfma_f32_16x16x32_bf16 v[22:25], v[6:9], v[38:41], v[14:17]
	ds_read_b128 v[6:9], v173 offset:48000
	s_waitcnt lgkmcnt(0)
	v_mfma_f32_16x16x32_bf16 v[18:21], v[6:9], v[38:41], v[18:21]
	ds_read_b128 v[6:9], v172 offset:52288
	s_waitcnt lgkmcnt(0)
	v_mfma_f32_16x16x32_bf16 v[14:17], v[6:9], v[38:41], v[42:45]
	ds_read_b128 v[6:9], v173 offset:56640
	s_nop 1
	ds_read_b128 v[42:45], v173 offset:65280
	s_waitcnt lgkmcnt(1)
	v_mfma_f32_16x16x32_bf16 v[10:13], v[6:9], v[38:41], v[46:49]
	ds_read_b128 v[6:9], v172 offset:60928
	v_lshl_add_u64 v[34:35], v[36:37], 2, s[0:1]
	s_movk_i32 s0, 0x1e00
	s_waitcnt lgkmcnt(0)
	v_mfma_f32_16x16x32_bf16 v[6:9], v[6:9], v[38:41], v[50:53]
	s_nop 2
	v_add_u32_e32 v50, s12, v36
	v_mov_b64_e32 v[36:37], s[38:39]
	v_mad_i64_i32 v[36:37], s[0:1], v50, s0, v[36:37]
	v_readlane_b32 s0, v253, 39
	s_lshl_b32 s0, s0, 1
	s_mov_b32 s1, s5
	v_lshl_add_u64 v[36:37], v[36:37], 0, s[0:1]
	v_lshl_add_u64 v[36:37], v[36:37], 0, v[206:207]
	v_mfma_f32_16x16x32_bf16 v[2:5], v[42:45], v[38:41], v[2:5]
	s_nop 0
	s_nop 0
	v_ashrrev_i32_e32 v51, 31, v50
	v_lshlrev_b64 v[50:51], 12, v[50:51]
	v_lshl_add_u64 v[50:51], s[36:37], 0, v[50:51]
	v_lshl_add_u64 v[50:51], v[50:51], 0, s[0:1]
	s_mov_b64 s[0:1], 0x2d1b8000
	s_waitcnt vmcnt(7)
	v_lshlrev_b32_e32 v54, 16, v120
	v_mul_f32_e32 v35, 0x3dd2d3e8, v54
	v_fma_f32 v35, -v35, v54, s33
	v_mul_f32_e32 v35, v35, v54
	v_exp_f32_e32 v35, v35
	v_and_b32_e32 v55, 0xffff0000, v120
	v_add_f32_e32 v35, 1.0, v35
	v_rcp_f32_e32 v56, v35
	v_mul_f32_e32 v35, 0x3dd2d3e8, v55
	v_fma_f32 v35, -v35, v55, s33
	v_mul_f32_e32 v35, v35, v55
	v_exp_f32_e32 v35, v35
	s_nop 0
	v_add_f32_e32 v35, 1.0, v35
	v_rcp_f32_e32 v57, v35
	v_pk_add_f32 v[30:31], v[30:31], v[136:137] op_sel_hi:[1, 0]
	v_pk_mul_f32 v[54:55], v[56:57], v[54:55]
	s_nop 0
	v_pk_mul_f32 v[30:31], v[30:31], v[54:55]
	s_nop 0
	v_cvt_pk_bf16_f32 v52, v30, v31
	v_lshlrev_b32_e32 v30, 16, v121
	v_mul_f32_e32 v35, 0x3dd2d3e8, v30
	v_fma_f32 v35, -v35, v30, s33
	v_mul_f32_e32 v35, v35, v30
	v_exp_f32_e32 v35, v35
	v_and_b32_e32 v31, 0xffff0000, v121
	v_add_f32_e32 v35, 1.0, v35
	v_rcp_f32_e32 v54, v35
	v_mul_f32_e32 v35, 0x3dd2d3e8, v31
	v_fma_f32 v35, -v35, v31, s33
	v_mul_f32_e32 v35, v35, v31
	v_exp_f32_e32 v35, v35
	s_nop 0
	v_add_f32_e32 v35, 1.0, v35
	v_rcp_f32_e32 v55, v35
	v_pk_add_f32 v[32:33], v[32:33], v[136:137] op_sel_hi:[1, 0]
	v_pk_mul_f32 v[30:31], v[54:55], v[30:31]
	s_nop 0
	v_pk_mul_f32 v[30:31], v[32:33], v[30:31]
	v_lshl_add_u64 v[32:33], v[50:51], 0, v[206:207]
	v_cvt_pk_bf16_f32 v53, v30, v31
	v_lshl_add_u64 v[30:31], v[32:33], 0, s[0:1]
	s_mov_b32 s0, 0x2d1b8000
	v_add_co_u32_e32 v32, vcc, s0, v32
	s_nop 1
	v_addc_co_u32_e32 v33, vcc, 0, v33, vcc
	global_store_dwordx2 v[32:33], v[52:53], off
	s_waitcnt vmcnt(7)
	v_lshlrev_b32_e32 v32, 16, v122
	v_mul_f32_e32 v35, 0x3dd2d3e8, v32
	v_fma_f32 v35, -v35, v32, s33
	v_mul_f32_e32 v35, v35, v32
	v_exp_f32_e32 v35, v35
	v_and_b32_e32 v33, 0xffff0000, v122
	v_add_f32_e32 v35, 1.0, v35
	v_rcp_f32_e32 v50, v35
	v_mul_f32_e32 v35, 0x3dd2d3e8, v33
	v_fma_f32 v35, -v35, v33, s33
	v_mul_f32_e32 v35, v35, v33
	v_exp_f32_e32 v35, v35
	s_nop 0
	v_add_f32_e32 v35, 1.0, v35
	v_rcp_f32_e32 v51, v35
	v_pk_add_f32 v[26:27], v[26:27], v[136:137] op_sel_hi:[1, 0]
	v_pk_add_f32 v[28:29], v[28:29], v[136:137] op_sel_hi:[1, 0]
	v_pk_add_f32 v[22:23], v[22:23], v[136:137] op_sel_hi:[1, 0]
	v_pk_mul_f32 v[32:33], v[50:51], v[32:33]
	v_pk_add_f32 v[24:25], v[24:25], v[136:137] op_sel_hi:[1, 0]
	v_pk_mul_f32 v[26:27], v[26:27], v[32:33]
	v_lshlrev_b32_e32 v32, 16, v123
	v_cvt_pk_bf16_f32 v26, v26, v27
	v_mul_f32_e32 v27, 0x3dd2d3e8, v32
	v_fma_f32 v27, -v27, v32, s33
	v_mul_f32_e32 v27, v27, v32
	v_exp_f32_e32 v27, v27
	v_and_b32_e32 v33, 0xffff0000, v123
	v_pk_add_f32 v[18:19], v[18:19], v[136:137] op_sel_hi:[1, 0]
	v_pk_add_f32 v[20:21], v[20:21], v[136:137] op_sel_hi:[1, 0]
	v_add_f32_e32 v27, 1.0, v27
	v_rcp_f32_e32 v48, v27
	v_mul_f32_e32 v27, 0x3dd2d3e8, v33
	v_fma_f32 v27, -v27, v33, s33
	v_mul_f32_e32 v27, v27, v33
	v_exp_f32_e32 v27, v27
	v_pk_add_f32 v[14:15], v[14:15], v[136:137] op_sel_hi:[1, 0]
	v_pk_add_f32 v[16:17], v[16:17], v[136:137] op_sel_hi:[1, 0]
	v_pk_add_f32 v[10:11], v[10:11], v[136:137] op_sel_hi:[1, 0]
	v_add_f32_e32 v27, 1.0, v27
	v_rcp_f32_e32 v49, v27
	v_pk_add_f32 v[12:13], v[12:13], v[136:137] op_sel_hi:[1, 0]
	v_pk_add_f32 v[6:7], v[6:7], v[136:137] op_sel_hi:[1, 0]
	v_pk_add_f32 v[8:9], v[8:9], v[136:137] op_sel_hi:[1, 0]
	v_pk_mul_f32 v[32:33], v[48:49], v[32:33]
	v_pk_add_f32 v[2:3], v[136:137], v[2:3] op_sel_hi:[0, 1]
	v_pk_mul_f32 v[28:29], v[28:29], v[32:33]
	v_pk_add_f32 v[4:5], v[136:137], v[4:5] op_sel_hi:[0, 1]
	v_cvt_pk_bf16_f32 v27, v28, v29
	global_store_dwordx2 v[30:31], v[26:27], off offset:32
	s_waitcnt vmcnt(7)
; __device__ __forceinline__ unsigned cvt_pk_bf16(float lo, float hi) { const f32x2 v = {lo, hi}; const bf16x2_t b = __builtin_convertvector(v, bf16x2_t); return __builtin_bit_cast(unsigned, b); }
; __device__ __forceinline__ float bflo(unsigned w) { return __uint_as_float(w << 16); }
; __device__ __forceinline__ float bfhi(unsigned w) { return __uint_as_float(w & 0xffff0000u); }
; __device__ __forceinline__ void sgu_unit(const Params& p, int l, int un, LAS unsigned char* lds) {
;     ...
;       for (int nb = 0; nb < 8; ++nb) { const int c = nb * 16 + 4 * fq; const u32x2 uv = uq[nb];
;           u32x2 w; w.x = cvt_pk_bf16(gelu_tanh(bflo(uv.x)) * (acc[nb][0] + bias), gelu_tanh(bfhi(uv.x)) * (acc[nb][1] + bias));
;           w.y = cvt_pk_bf16(gelu_tanh(bflo(uv.y)) * (acc[nb][2] + bias), gelu_tanh(bfhi(uv.y)) * (acc[nb][3] + bias));
;           *(u32x2*)(CAT + (size_t)(row0 + pp) * DM + h * 128 + c) = w; } }
	v_lshlrev_b32_e32 v26, 16, v124
	v_and_b32_e32 v27, 0xffff0000, v124
	v_mul_f32_e32 v28, 0x3dd2d3e8, v26
	v_mul_f32_e32 v29, 0x3dd2d3e8, v27
	v_fma_f32 v28, -v28, v26, s33
	v_fma_f32 v29, -v29, v27, s33
	v_mul_f32_e32 v28, v28, v26
	v_mul_f32_e32 v29, v29, v27
	v_exp_f32_e32 v28, v28
	v_exp_f32_e32 v29, v29
	v_add_f32_e32 v28, 1.0, v28
	v_add_f32_e32 v29, 1.0, v29
	v_rcp_f32_e32 v28, v28
	v_rcp_f32_e32 v29, v29
	s_nop 0
	v_pk_mul_f32 v[26:27], v[28:29], v[26:27]
	s_nop 0
	v_pk_mul_f32 v[22:23], v[22:23], v[26:27]
	v_lshlrev_b32_e32 v26, 16, v125
	v_cvt_pk_bf16_f32 v22, v22, v23
	v_mul_f32_e32 v23, 0x3dd2d3e8, v26
	v_fma_f32 v23, -v23, v26, s33
	v_mul_f32_e32 v23, v23, v26
	v_exp_f32_e32 v23, v23
	v_and_b32_e32 v27, 0xffff0000, v125
	v_add_f32_e32 v23, 1.0, v23
	v_rcp_f32_e32 v28, v23
	v_mul_f32_e32 v23, 0x3dd2d3e8, v27
	v_fma_f32 v23, -v23, v27, s33
	v_mul_f32_e32 v23, v23, v27
	v_exp_f32_e32 v23, v23
	s_nop 0
	v_add_f32_e32 v23, 1.0, v23
	v_rcp_f32_e32 v29, v23
	s_nop 0
	v_pk_mul_f32 v[26:27], v[28:29], v[26:27]
	s_nop 0
	v_pk_mul_f32 v[24:25], v[24:25], v[26:27]
	s_nop 0
	v_cvt_pk_bf16_f32 v23, v24, v25
	global_store_dwordx2 v[30:31], v[22:23], off offset:64
	s_waitcnt vmcnt(7)
	v_lshlrev_b32_e32 v22, 16, v126
	v_and_b32_e32 v23, 0xffff0000, v126
	v_mul_f32_e32 v24, 0x3dd2d3e8, v22
	v_mul_f32_e32 v25, 0x3dd2d3e8, v23
	v_fma_f32 v24, -v24, v22, s33
	v_fma_f32 v25, -v25, v23, s33
	v_mul_f32_e32 v24, v24, v22
	v_mul_f32_e32 v25, v25, v23
	v_exp_f32_e32 v24, v24
	v_exp_f32_e32 v25, v25
	v_add_f32_e32 v24, 1.0, v24
	v_add_f32_e32 v25, 1.0, v25
	v_rcp_f32_e32 v24, v24
	v_rcp_f32_e32 v25, v25
	s_nop 0
	v_pk_mul_f32 v[22:23], v[24:25], v[22:23]
	s_nop 0
	v_pk_mul_f32 v[18:19], v[18:19], v[22:23]
	v_lshlrev_b32_e32 v22, 16, v127
	v_cvt_pk_bf16_f32 v18, v18, v19
	v_mul_f32_e32 v19, 0x3dd2d3e8, v22
	v_fma_f32 v19, -v19, v22, s33
	v_mul_f32_e32 v19, v19, v22
	v_exp_f32_e32 v19, v19
	v_and_b32_e32 v23, 0xffff0000, v127
	v_add_f32_e32 v19, 1.0, v19
	v_rcp_f32_e32 v24, v19
	v_mul_f32_e32 v19, 0x3dd2d3e8, v23
	v_fma_f32 v19, -v19, v23, s33
	v_mul_f32_e32 v19, v19, v23
	v_exp_f32_e32 v19, v19
	s_nop 0
	v_add_f32_e32 v19, 1.0, v19
	v_rcp_f32_e32 v25, v19
	s_nop 0
	v_pk_mul_f32 v[22:23], v[24:25], v[22:23]
	s_nop 0
	v_pk_mul_f32 v[20:21], v[20:21], v[22:23]
	s_nop 0
	v_cvt_pk_bf16_f32 v19, v20, v21
	global_store_dwordx2 v[30:31], v[18:19], off offset:96
	s_waitcnt vmcnt(7)
	v_lshlrev_b32_e32 v18, 16, v128
	v_and_b32_e32 v19, 0xffff0000, v128
	v_mul_f32_e32 v20, 0x3dd2d3e8, v18
	v_mul_f32_e32 v21, 0x3dd2d3e8, v19
	v_fma_f32 v20, -v20, v18, s33
	v_fma_f32 v21, -v21, v19, s33
	v_mul_f32_e32 v20, v20, v18
	v_mul_f32_e32 v21, v21, v19
	v_exp_f32_e32 v20, v20
	v_exp_f32_e32 v21, v21
	v_add_f32_e32 v20, 1.0, v20
	v_add_f32_e32 v21, 1.0, v21
	v_rcp_f32_e32 v20, v20
	v_rcp_f32_e32 v21, v21
	s_nop 0
	v_pk_mul_f32 v[18:19], v[20:21], v[18:19]
	s_nop 0
	v_pk_mul_f32 v[14:15], v[14:15], v[18:19]
	v_lshlrev_b32_e32 v18, 16, v129
	v_cvt_pk_bf16_f32 v14, v14, v15
	v_mul_f32_e32 v15, 0x3dd2d3e8, v18
	v_fma_f32 v15, -v15, v18, s33
	v_mul_f32_e32 v15, v15, v18
	v_exp_f32_e32 v15, v15
	v_and_b32_e32 v19, 0xffff0000, v129
	v_add_f32_e32 v15, 1.0, v15
	v_rcp_f32_e32 v20, v15
	v_mul_f32_e32 v15, 0x3dd2d3e8, v19
	v_fma_f32 v15, -v15, v19, s33
	v_mul_f32_e32 v15, v15, v19
	v_exp_f32_e32 v15, v15
	s_nop 0
	v_add_f32_e32 v15, 1.0, v15
	v_rcp_f32_e32 v21, v15
	s_nop 0
	v_pk_mul_f32 v[18:19], v[20:21], v[18:19]
	s_nop 0
	v_pk_mul_f32 v[16:17], v[16:17], v[18:19]
	s_nop 0
	v_cvt_pk_bf16_f32 v15, v16, v17
	global_store_dwordx2 v[30:31], v[14:15], off offset:128
	s_waitcnt vmcnt(7)
; __device__ __forceinline__ unsigned cvt_pk_bf16(float lo, float hi) { const f32x2 v = {lo, hi}; const bf16x2_t b = __builtin_convertvector(v, bf16x2_t); return __builtin_bit_cast(unsigned, b); }
; __device__ __forceinline__ float bflo(unsigned w) { return __uint_as_float(w << 16); }
; __device__ __forceinline__ float bfhi(unsigned w) { return __uint_as_float(w & 0xffff0000u); }
; __device__ __forceinline__ void sgu_unit(const Params& p, int l, int un, LAS unsigned char* lds) {
;     ...
;       for (int nb = 0; nb < 8; ++nb) { const int c = nb * 16 + 4 * fq; const u32x2 uv = uq[nb];
;           u32x2 w; w.x = cvt_pk_bf16(gelu_tanh(bflo(uv.x)) * (acc[nb][0] + bias), gelu_tanh(bfhi(uv.x)) * (acc[nb][1] + bias));
;           w.y = cvt_pk_bf16(gelu_tanh(bflo(uv.y)) * (acc[nb][2] + bias), gelu_tanh(bfhi(uv.y)) * (acc[nb][3] + bias));
;           *(u32x2*)(CAT + (size_t)(row0 + pp) * DM + h * 128 + c) = w; } }
	v_lshlrev_b32_e32 v14, 16, v130
	v_and_b32_e32 v15, 0xffff0000, v130
	v_mul_f32_e32 v16, 0x3dd2d3e8, v14
	v_mul_f32_e32 v17, 0x3dd2d3e8, v15
	v_fma_f32 v16, -v16, v14, s33
	v_fma_f32 v17, -v17, v15, s33
	v_mul_f32_e32 v16, v16, v14
	v_mul_f32_e32 v17, v17, v15
	v_exp_f32_e32 v16, v16
	v_exp_f32_e32 v17, v17
	v_add_f32_e32 v16, 1.0, v16
	v_add_f32_e32 v17, 1.0, v17
	v_rcp_f32_e32 v16, v16
	v_rcp_f32_e32 v17, v17
	s_nop 0
	v_pk_mul_f32 v[14:15], v[16:17], v[14:15]
	s_nop 0
	v_pk_mul_f32 v[10:11], v[10:11], v[14:15]
	v_lshlrev_b32_e32 v14, 16, v131
	v_cvt_pk_bf16_f32 v10, v10, v11
	v_mul_f32_e32 v11, 0x3dd2d3e8, v14
	v_fma_f32 v11, -v11, v14, s33
	v_mul_f32_e32 v11, v11, v14
	v_exp_f32_e32 v11, v11
	v_and_b32_e32 v15, 0xffff0000, v131
	v_add_f32_e32 v11, 1.0, v11
	v_rcp_f32_e32 v16, v11
	v_mul_f32_e32 v11, 0x3dd2d3e8, v15
	v_fma_f32 v11, -v11, v15, s33
	v_mul_f32_e32 v11, v11, v15
	v_exp_f32_e32 v11, v11
	s_nop 0
	v_add_f32_e32 v11, 1.0, v11
	v_rcp_f32_e32 v17, v11
	s_nop 0
	v_pk_mul_f32 v[14:15], v[16:17], v[14:15]
	s_nop 0
	v_pk_mul_f32 v[12:13], v[12:13], v[14:15]
	s_nop 0
	v_cvt_pk_bf16_f32 v11, v12, v13
	global_store_dwordx2 v[30:31], v[10:11], off offset:160
	s_waitcnt vmcnt(7)
	v_lshlrev_b32_e32 v10, 16, v132
	v_and_b32_e32 v11, 0xffff0000, v132
	v_mul_f32_e32 v12, 0x3dd2d3e8, v10
	v_mul_f32_e32 v13, 0x3dd2d3e8, v11
	v_fma_f32 v12, -v12, v10, s33
	v_fma_f32 v13, -v13, v11, s33
	v_mul_f32_e32 v12, v12, v10
	v_mul_f32_e32 v13, v13, v11
	v_exp_f32_e32 v12, v12
	v_exp_f32_e32 v13, v13
	v_add_f32_e32 v12, 1.0, v12
	v_add_f32_e32 v13, 1.0, v13
	v_rcp_f32_e32 v12, v12
	v_rcp_f32_e32 v13, v13
	s_nop 0
	v_pk_mul_f32 v[10:11], v[12:13], v[10:11]
	s_nop 0
	v_pk_mul_f32 v[6:7], v[6:7], v[10:11]
	v_lshlrev_b32_e32 v10, 16, v133
	v_cvt_pk_bf16_f32 v6, v6, v7
	v_mul_f32_e32 v7, 0x3dd2d3e8, v10
	v_fma_f32 v7, -v7, v10, s33
	v_mul_f32_e32 v7, v7, v10
	v_exp_f32_e32 v7, v7
	v_and_b32_e32 v11, 0xffff0000, v133
	v_add_f32_e32 v7, 1.0, v7
	v_rcp_f32_e32 v12, v7
	v_mul_f32_e32 v7, 0x3dd2d3e8, v11
	v_fma_f32 v7, -v7, v11, s33
	v_mul_f32_e32 v7, v7, v11
	v_exp_f32_e32 v7, v7
	s_nop 0
	v_add_f32_e32 v7, 1.0, v7
	v_rcp_f32_e32 v13, v7
	s_nop 0
	v_pk_mul_f32 v[10:11], v[12:13], v[10:11]
	s_nop 0
	v_pk_mul_f32 v[8:9], v[8:9], v[10:11]
	s_nop 0
	v_cvt_pk_bf16_f32 v7, v8, v9
	global_store_dwordx2 v[30:31], v[6:7], off offset:192
	s_waitcnt vmcnt(7)
	v_lshlrev_b32_e32 v6, 16, v134
	v_and_b32_e32 v7, 0xffff0000, v134
	v_mul_f32_e32 v8, 0x3dd2d3e8, v6
	v_mul_f32_e32 v9, 0x3dd2d3e8, v7
	v_fma_f32 v8, -v8, v6, s33
	v_fma_f32 v9, -v9, v7, s33
	v_mul_f32_e32 v8, v8, v6
	v_mul_f32_e32 v9, v9, v7
	v_exp_f32_e32 v8, v8
	v_exp_f32_e32 v9, v9
	v_add_f32_e32 v8, 1.0, v8
	v_add_f32_e32 v9, 1.0, v9
	v_rcp_f32_e32 v8, v8
	v_rcp_f32_e32 v9, v9
	s_nop 0
	v_pk_mul_f32 v[6:7], v[8:9], v[6:7]
	s_nop 0
	v_pk_mul_f32 v[2:3], v[2:3], v[6:7]
	v_lshlrev_b32_e32 v6, 16, v135
	v_cvt_pk_bf16_f32 v2, v2, v3
	v_mul_f32_e32 v3, 0x3dd2d3e8, v6
	v_fma_f32 v3, -v3, v6, s33
	v_mul_f32_e32 v3, v3, v6
	v_exp_f32_e32 v3, v3
	v_and_b32_e32 v7, 0xffff0000, v135
	v_add_f32_e32 v3, 1.0, v3
	v_rcp_f32_e32 v8, v3
	v_mul_f32_e32 v3, 0x3dd2d3e8, v7
	v_fma_f32 v3, -v3, v7, s33
	v_mul_f32_e32 v3, v3, v7
	v_exp_f32_e32 v3, v3
	s_nop 0
	v_add_f32_e32 v3, 1.0, v3
	v_rcp_f32_e32 v9, v3
	s_nop 0
	v_pk_mul_f32 v[6:7], v[8:9], v[6:7]
	s_nop 0
	v_pk_mul_f32 v[4:5], v[4:5], v[6:7]
	s_nop 0
	v_cvt_pk_bf16_f32 v3, v4, v5
	global_store_dwordx2 v[30:31], v[2:3], off offset:224
	s_barrier

; #define LAS __attribute__((address_space(3)))
; __device__ __forceinline__ void sgu_unit(const Params& p, int l, int un, LAS unsigned char* lds) {
;     ...
;     __syncthreads();
;     { const int fr = lane & 15, fq = lane >> 4; f32x4 acc[8];
; #pragma unroll
;       for (int nb = 0; nb < 8; ++nb) acc[nb] = (f32x4){0.f, 0.f, 0.f, 0.f};
; #pragma unroll
;       for (int ks = 0; ks < 4; ++ks) { const bf16x8 af = *(const LAS bf16x8*)(Wl + (wave * 16 + fr) * 136 + ks * 32 + fq * 8);
; #pragma unroll
;           for (int nb = 0; nb < 8; ++nb) { const bf16x8 bfr = *(const LAS bf16x8*)(Vl + (nb * 16 + fr) * 136 + ks * 32 + fq * 8);
;               acc[nb] = __builtin_amdgcn_mfma_f32_16x16x32_bf16(bfr, af, acc[nb], 0, 0, 0); } }
;       const int pp = wave * 16 + fr; const float bias = p.in[I_SGUB][((size_t)l * 4 + h) * 128 + pp]; const bf16_t* pr = P + (size_t)(row0 + pp) * INP + C_SGU_U + h * 128;
;       u32x2 uq[8];
; #pragma unroll
;       for (int nb = 0; nb < 8; ++nb) uq[nb] = *(const u32x2*)(pr + nb * 16 + 4 * fq);
.LBB0_1428:
	s_or_b64 exec, exec, s[0:1]
	v_and_b32_e32 v7, 15, v64
	v_or_b32_e32 v36, v65, v7
	v_lshl_add_u32 v6, v66, 4, 0
	v_mad_u64_u32 v[34:35], s[2:3], v36, s13, v[6:7]
	v_mad_u32_u24 v35, v7, s13, v6
	v_bfe_u32 v170, v0, 4, 2
	v_bfe_u32 v171, v0, 3, 1
	v_xor_b32_e32 v172, v170, v171
	v_sub_u32_e32 v172, v172, v170
	v_lshl_add_u32 v172, v172, 4, v35
	v_xor_b32_e32 v173, 2, v170
	v_xor_b32_e32 v173, v173, v171
	v_sub_u32_e32 v173, v173, v170
	v_lshl_add_u32 v173, v173, 4, v35
	v_ashrrev_i32_e32 v139, 31, v36
	v_mov_b32_e32 v138, v36
	s_lshl_b64 s[0:1], s[40:41], 2
	v_readlane_b32 s2, v251, 24
	v_readlane_b32 s3, v251, 25
	s_add_u32 s0, s2, s0
	s_addc_u32 s1, s3, s1
	v_lshl_add_u64 v[140:141], v[138:139], 2, s[0:1]
	global_load_dword v136, v[140:141], off
	s_movk_i32 s0, 0x1e00
	v_add_u32_e32 v137, s12, v36
	v_mov_b64_e32 v[140:141], s[38:39]
	v_mad_i64_i32 v[140:141], s[0:1], v137, s0, v[140:141]
	v_readlane_b32 s0, v253, 39
	s_lshl_b32 s0, s0, 1
	s_mov_b32 s1, s5
	v_lshlrev_b32_e32 v142, 3, v66
	v_mov_b32_e32 v143, 0
	v_lshl_add_u64 v[140:141], v[140:141], 0, s[0:1]
	v_lshl_add_u64 v[140:141], v[140:141], 0, v[142:143]
	global_load_dwordx2 v[120:121], v[140:141], off
	global_load_dwordx2 v[122:123], v[140:141], off offset:32
	global_load_dwordx2 v[124:125], v[140:141], off offset:64
	global_load_dwordx2 v[126:127], v[140:141], off offset:96
	global_load_dwordx2 v[128:129], v[140:141], off offset:128
	global_load_dwordx2 v[130:131], v[140:141], off offset:160
	global_load_dwordx2 v[132:133], v[140:141], off offset:192
	global_load_dwordx2 v[134:135], v[140:141], off offset:224
	s_waitcnt lgkmcnt(0)
	s_barrier
	ds_read_b128 v[2:5], v34
	ds_read_b128 v[6:9], v172 offset:34816
	ds_read_b128 v[10:13], v173 offset:39168
	ds_read_b128 v[14:17], v172 offset:43584
	ds_read_b128 v[18:21], v173 offset:47936
	ds_read_b128 v[22:25], v172 offset:52352
	ds_read_b128 v[26:29], v173 offset:56704
	ds_read_b128 v[30:33], v172 offset:61120
	ds_read_b128 v[38:41], v173 offset:65472
	s_waitcnt lgkmcnt(7)
	v_mfma_f32_16x16x32_bf16 v[6:9], v[6:9], v[2:5], 0
	s_lshl_b64 s[0:1], s[40:41], 2
	v_readlane_b32 s40, v251, 16
	v_readlane_b32 s44, v251, 20
	s_waitcnt lgkmcnt(6)
	v_mfma_f32_16x16x32_bf16 v[10:13], v[10:13], v[2:5], 0
	v_readlane_b32 s45, v251, 21
	v_readlane_b32 s46, v251, 22
	v_readlane_b32 s47, v251, 23
	s_waitcnt lgkmcnt(5)
	v_mfma_f32_16x16x32_bf16 v[14:17], v[14:17], v[2:5], 0
	v_readlane_b32 s48, v251, 24
	v_readlane_b32 s49, v251, 25
	v_readlane_b32 s50, v251, 26
	s_waitcnt lgkmcnt(4)
	v_mfma_f32_16x16x32_bf16 v[18:21], v[18:21], v[2:5], 0
	v_readlane_b32 s51, v251, 27
	s_mov_b64 s[16:17], s[44:45]
	s_mov_b64 s[20:21], s[48:49]
	s_waitcnt lgkmcnt(3)
	v_mfma_f32_16x16x32_bf16 v[22:25], v[22:25], v[2:5], 0
	s_add_u32 s0, s20, s0
	s_addc_u32 s1, s21, s1
	v_ashrrev_i32_e32 v37, 31, v36
	s_waitcnt lgkmcnt(2)
	v_mfma_f32_16x16x32_bf16 v[26:29], v[26:29], v[2:5], 0
	v_lshlrev_b32_e32 v206, 3, v66
	v_readlane_b32 s41, v251, 17
	v_readlane_b32 s42, v251, 18
	s_waitcnt lgkmcnt(1)
	v_mfma_f32_16x16x32_bf16 v[30:33], v[30:33], v[2:5], 0
	v_readlane_b32 s43, v251, 19
	v_readlane_b32 s52, v251, 28
	v_readlane_b32 s53, v251, 29
	s_waitcnt lgkmcnt(0)
	v_mfma_f32_16x16x32_bf16 v[2:5], v[38:41], v[2:5], 0
	ds_read_b128 v[38:41], v34 offset:64
	ds_read_b128 v[42:45], v172 offset:34880
	v_readlane_b32 s54, v251, 30
	v_readlane_b32 s55, v251, 31
	s_waitcnt lgkmcnt(0)
	v_mfma_f32_16x16x32_bf16 v[6:9], v[42:45], v[38:41], v[6:9]
	ds_read_b128 v[42:45], v173 offset:39232
	s_mov_b64 s[18:19], s[46:47]
	s_mov_b64 s[22:23], s[50:51]
	s_waitcnt lgkmcnt(0)
	v_mfma_f32_16x16x32_bf16 v[10:13], v[42:45], v[38:41], v[10:13]
	ds_read_b128 v[42:45], v172 offset:43520
	s_waitcnt lgkmcnt(0)
	v_mfma_f32_16x16x32_bf16 v[14:17], v[42:45], v[38:41], v[14:17]
	ds_read_b128 v[42:45], v173 offset:47872
	s_waitcnt lgkmcnt(0)
	v_mfma_f32_16x16x32_bf16 v[18:21], v[42:45], v[38:41], v[18:21]
	ds_read_b128 v[42:45], v172 offset:52416
	s_waitcnt lgkmcnt(0)
	v_mfma_f32_16x16x32_bf16 v[22:25], v[42:45], v[38:41], v[22:25]
	ds_read_b128 v[42:45], v173 offset:56768
	s_waitcnt lgkmcnt(0)
	v_mfma_f32_16x16x32_bf16 v[26:29], v[42:45], v[38:41], v[26:29]
	ds_read_b128 v[42:45], v172 offset:61056
	s_waitcnt lgkmcnt(0)
	v_mfma_f32_16x16x32_bf16 v[30:33], v[42:45], v[38:41], v[30:33]
	ds_read_b128 v[42:45], v173 offset:65408
	s_waitcnt lgkmcnt(0)
	v_mfma_f32_16x16x32_bf16 v[2:5], v[42:45], v[38:41], v[2:5]
	ds_read_b128 v[38:41], v34 offset:128
	ds_read_b128 v[42:45], v172 offset:34944
	s_waitcnt lgkmcnt(0)
	v_mfma_f32_16x16x32_bf16 v[6:9], v[42:45], v[38:41], v[6:9]
	ds_read_b128 v[42:45], v173 offset:39296
	s_waitcnt lgkmcnt(0)
	v_mfma_f32_16x16x32_bf16 v[10:13], v[42:45], v[38:41], v[10:13]
	ds_read_b128 v[42:45], v172 offset:43712
	s_waitcnt lgkmcnt(0)
	v_mfma_f32_16x16x32_bf16 v[14:17], v[42:45], v[38:41], v[14:17]
	ds_read_b128 v[42:45], v173 offset:48064
	s_waitcnt lgkmcnt(0)
	v_mfma_f32_16x16x32_bf16 v[18:21], v[42:45], v[38:41], v[18:21]
	ds_read_b128 v[42:45], v172 offset:52224
	s_waitcnt lgkmcnt(0)
	v_mfma_f32_16x16x32_bf16 v[42:45], v[42:45], v[38:41], v[22:25]
	s_nop 2
	ds_read_b128 v[22:25], v173 offset:56576
	s_waitcnt lgkmcnt(0)
	v_mfma_f32_16x16x32_bf16 v[46:49], v[22:25], v[38:41], v[26:29]
	ds_read_b128 v[22:25], v172 offset:60992
	s_waitcnt lgkmcnt(0)
	v_mfma_f32_16x16x32_bf16 v[50:53], v[22:25], v[38:41], v[30:33]
	ds_read_b128 v[22:25], v173 offset:65344
	s_waitcnt lgkmcnt(0)
	v_mfma_f32_16x16x32_bf16 v[2:5], v[22:25], v[38:41], v[2:5]
	ds_read_b128 v[38:41], v34 offset:192
	ds_read_b128 v[22:25], v172 offset:35008
	s_waitcnt lgkmcnt(0)
; #define LAS __attribute__((address_space(3)))
; __device__ __forceinline__ unsigned cvt_pk_bf16(float lo, float hi) { const f32x2 v = {lo, hi}; const bf16x2_t b = __builtin_convertvector(v, bf16x2_t); return __builtin_bit_cast(unsigned, b); }
; __device__ __forceinline__ float bflo(unsigned w) { return __uint_as_float(w << 16); }
; __device__ __forceinline__ float bfhi(unsigned w) { return __uint_as_float(w & 0xffff0000u); }
; __device__ __forceinline__ void sgu_unit(const Params& p, int l, int un, LAS unsigned char* lds) {
;     ...
;       for (int ks = 0; ks < 4; ++ks) { const bf16x8 af = *(const LAS bf16x8*)(Wl + (wave * 16 + fr) * 136 + ks * 32 + fq * 8);
; #pragma unroll
;           for (int nb = 0; nb < 8; ++nb) { const bf16x8 bfr = *(const LAS bf16x8*)(Vl + (nb * 16 + fr) * 136 + ks * 32 + fq * 8);
;               acc[nb] = __builtin_amdgcn_mfma_f32_16x16x32_bf16(bfr, af, acc[nb], 0, 0, 0); } }
;       const int pp = wave * 16 + fr; const float bias = p.in[I_SGUB][((size_t)l * 4 + h) * 128 + pp]; const bf16_t* pr = P + (size_t)(row0 + pp) * INP + C_SGU_U + h * 128;
;       u32x2 uq[8];
; #pragma unroll
;       for (int nb = 0; nb < 8; ++nb) uq[nb] = *(const u32x2*)(pr + nb * 16 + 4 * fq);
; #pragma unroll
;       for (int nb = 0; nb < 8; ++nb) { const int c = nb * 16 + 4 * fq; const u32x2 uv = uq[nb];
;           u32x2 w; w.x = cvt_pk_bf16(gelu_tanh(bflo(uv.x)) * (acc[nb][0] + bias), gelu_tanh(bfhi(uv.x)) * (acc[nb][1] + bias));
;           w.y = cvt_pk_bf16(gelu_tanh(bflo(uv.y)) * (acc[nb][2] + bias), gelu_tanh(bfhi(uv.y)) * (acc[nb][3] + bias));
;           *(u32x2*)(CAT + (size_t)(row0 + pp) * DM + h * 128 + c) = w; } }
	v_mfma_f32_16x16x32_bf16 v[30:33], v[22:25], v[38:41], v[6:9]
	s_nop 2
	ds_read_b128 v[6:9], v173 offset:39360
	s_waitcnt lgkmcnt(0)
	v_mfma_f32_16x16x32_bf16 v[26:29], v[6:9], v[38:41], v[10:13]
	ds_read_b128 v[6:9], v172 offset:43648
	s_waitcnt lgkmcnt(0)
	v_mfma_f32_16x16x32_bf16 v[22:25], v[6:9], v[38:41], v[14:17]
	ds_read_b128 v[6:9], v173 offset:48000
	s_waitcnt lgkmcnt(0)
	v_mfma_f32_16x16x32_bf16 v[18:21], v[6:9], v[38:41], v[18:21]
	ds_read_b128 v[6:9], v172 offset:52288
	s_waitcnt lgkmcnt(0)
	v_mfma_f32_16x16x32_bf16 v[14:17], v[6:9], v[38:41], v[42:45]
	ds_read_b128 v[6:9], v173 offset:56640
	s_nop 1
	ds_read_b128 v[42:45], v173 offset:65280
	s_waitcnt lgkmcnt(1)
	v_mfma_f32_16x16x32_bf16 v[10:13], v[6:9], v[38:41], v[46:49]
	ds_read_b128 v[6:9], v172 offset:60928
	v_lshl_add_u64 v[34:35], v[36:37], 2, s[0:1]
	s_movk_i32 s0, 0x1e00
	s_waitcnt lgkmcnt(0)
	v_mfma_f32_16x16x32_bf16 v[6:9], v[6:9], v[38:41], v[50:53]
	s_nop 2
	v_add_u32_e32 v50, s12, v36
	v_mov_b64_e32 v[36:37], s[38:39]
	v_mad_i64_i32 v[36:37], s[0:1], v50, s0, v[36:37]
	v_readlane_b32 s0, v253, 39
	s_lshl_b32 s0, s0, 1
	s_mov_b32 s1, s5
	v_lshl_add_u64 v[36:37], v[36:37], 0, s[0:1]
	v_lshl_add_u64 v[36:37], v[36:37], 0, v[206:207]
	v_mfma_f32_16x16x32_bf16 v[2:5], v[42:45], v[38:41], v[2:5]
	s_nop 0
	s_nop 0
	v_ashrrev_i32_e32 v51, 31, v50
	v_lshlrev_b64 v[50:51], 12, v[50:51]
	v_lshl_add_u64 v[50:51], s[36:37], 0, v[50:51]
	v_lshl_add_u64 v[50:51], v[50:51], 0, s[0:1]
	s_mov_b64 s[0:1], 0x2d1b8000
	s_waitcnt vmcnt(7)
	v_lshlrev_b32_e32 v54, 16, v120
	v_mul_f32_e32 v35, 0x3dd2d3e8, v54
	v_fma_f32 v35, -v35, v54, s33
	v_mul_f32_e32 v35, v35, v54
	v_exp_f32_e32 v35, v35
	v_and_b32_e32 v55, 0xffff0000, v120
	v_add_f32_e32 v35, 1.0, v35
	v_rcp_f32_e32 v56, v35
	v_mul_f32_e32 v35, 0x3dd2d3e8, v55
	v_fma_f32 v35, -v35, v55, s33
	v_mul_f32_e32 v35, v35, v55
	v_exp_f32_e32 v35, v35
	s_nop 0
	v_add_f32_e32 v35, 1.0, v35
	v_rcp_f32_e32 v57, v35
	v_pk_add_f32 v[30:31], v[30:31], v[136:137] op_sel_hi:[1, 0]
	v_pk_mul_f32 v[54:55], v[56:57], v[54:55]
	s_nop 0
	v_pk_mul_f32 v[30:31], v[30:31], v[54:55]
	s_nop 0
	v_cvt_pk_bf16_f32 v52, v30, v31
	v_lshlrev_b32_e32 v30, 16, v121
	v_mul_f32_e32 v35, 0x3dd2d3e8, v30
	v_fma_f32 v35, -v35, v30, s33
	v_mul_f32_e32 v35, v35, v30
	v_exp_f32_e32 v35, v35
	v_and_b32_e32 v31, 0xffff0000, v121
	v_add_f32_e32 v35, 1.0, v35
	v_rcp_f32_e32 v54, v35
	v_mul_f32_e32 v35, 0x3dd2d3e8, v31
	v_fma_f32 v35, -v35, v31, s33
	v_mul_f32_e32 v35, v35, v31
	v_exp_f32_e32 v35, v35
	s_nop 0
	v_add_f32_e32 v35, 1.0, v35
	v_rcp_f32_e32 v55, v35
	v_pk_add_f32 v[32:33], v[32:33], v[136:137] op_sel_hi:[1, 0]
	v_pk_mul_f32 v[30:31], v[54:55], v[30:31]
	s_nop 0
	v_pk_mul_f32 v[30:31], v[32:33], v[30:31]
	v_lshl_add_u64 v[32:33], v[50:51], 0, v[206:207]
	v_cvt_pk_bf16_f32 v53, v30, v31
	v_lshl_add_u64 v[30:31], v[32:33], 0, s[0:1]
	s_mov_b32 s0, 0x2d1b8000
	v_add_co_u32_e32 v32, vcc, s0, v32
	s_nop 1
	v_addc_co_u32_e32 v33, vcc, 0, v33, vcc
	global_store_dwordx2 v[32:33], v[52:53], off
	s_waitcnt vmcnt(7)
	v_lshlrev_b32_e32 v32, 16, v122
	v_mul_f32_e32 v35, 0x3dd2d3e8, v32
	v_fma_f32 v35, -v35, v32, s33
	v_mul_f32_e32 v35, v35, v32
	v_exp_f32_e32 v35, v35
	v_and_b32_e32 v33, 0xffff0000, v122
	v_add_f32_e32 v35, 1.0, v35
	v_rcp_f32_e32 v50, v35
	v_mul_f32_e32 v35, 0x3dd2d3e8, v33
	v_fma_f32 v35, -v35, v33, s33
	v_mul_f32_e32 v35, v35, v33
	v_exp_f32_e32 v35, v35
	s_nop 0
	v_add_f32_e32 v35, 1.0, v35
	v_rcp_f32_e32 v51, v35
	v_pk_add_f32 v[26:27], v[26:27], v[136:137] op_sel_hi:[1, 0]
	v_pk_add_f32 v[28:29], v[28:29], v[136:137] op_sel_hi:[1, 0]
	v_pk_add_f32 v[22:23], v[22:23], v[136:137] op_sel_hi:[1, 0]
	v_pk_mul_f32 v[32:33], v[50:51], v[32:33]
	v_pk_add_f32 v[24:25], v[24:25], v[136:137] op_sel_hi:[1, 0]
	v_pk_mul_f32 v[26:27], v[26:27], v[32:33]
	v_lshlrev_b32_e32 v32, 16, v123
	v_cvt_pk_bf16_f32 v26, v26, v27
	v_mul_f32_e32 v27, 0x3dd2d3e8, v32
	v_fma_f32 v27, -v27, v32, s33
	v_mul_f32_e32 v27, v27, v32
	v_exp_f32_e32 v27, v27
	v_and_b32_e32 v33, 0xffff0000, v123
	v_pk_add_f32 v[18:19], v[18:19], v[136:137] op_sel_hi:[1, 0]
	v_pk_add_f32 v[20:21], v[20:21], v[136:137] op_sel_hi:[1, 0]
	v_add_f32_e32 v27, 1.0, v27
	v_rcp_f32_e32 v48, v27
	v_mul_f32_e32 v27, 0x3dd2d3e8, v33
	v_fma_f32 v27, -v27, v33, s33
	v_mul_f32_e32 v27, v27, v33
	v_exp_f32_e32 v27, v27
	v_pk_add_f32 v[14:15], v[14:15], v[136:137] op_sel_hi:[1, 0]
	v_pk_add_f32 v[16:17], v[16:17], v[136:137] op_sel_hi:[1, 0]
	v_pk_add_f32 v[10:11], v[10:11], v[136:137] op_sel_hi:[1, 0]
	v_add_f32_e32 v27, 1.0, v27
	v_rcp_f32_e32 v49, v27
	v_pk_add_f32 v[12:13], v[12:13], v[136:137] op_sel_hi:[1, 0]
	v_pk_add_f32 v[6:7], v[6:7], v[136:137] op_sel_hi:[1, 0]
	v_pk_add_f32 v[8:9], v[8:9], v[136:137] op_sel_hi:[1, 0]
	v_pk_mul_f32 v[32:33], v[48:49], v[32:33]
	v_pk_add_f32 v[2:3], v[136:137], v[2:3] op_sel_hi:[0, 1]
	v_pk_mul_f32 v[28:29], v[28:29], v[32:33]
	v_pk_add_f32 v[4:5], v[136:137], v[4:5] op_sel_hi:[0, 1]
	v_cvt_pk_bf16_f32 v27, v28, v29
	global_store_dwordx2 v[30:31], v[26:27], off offset:32
	s_waitcnt vmcnt(7)
; __device__ __forceinline__ unsigned cvt_pk_bf16(float lo, float hi) { const f32x2 v = {lo, hi}; const bf16x2_t b = __builtin_convertvector(v, bf16x2_t); return __builtin_bit_cast(unsigned, b); }
; __device__ __forceinline__ float bflo(unsigned w) { return __uint_as_float(w << 16); }
; __device__ __forceinline__ float bfhi(unsigned w) { return __uint_as_float(w & 0xffff0000u); }
; __device__ __forceinline__ void sgu_unit(const Params& p, int l, int un, LAS unsigned char* lds) {
;     ...
;       for (int nb = 0; nb < 8; ++nb) { const int c = nb * 16 + 4 * fq; const u32x2 uv = uq[nb];
;           u32x2 w; w.x = cvt_pk_bf16(gelu_tanh(bflo(uv.x)) * (acc[nb][0] + bias), gelu_tanh(bfhi(uv.x)) * (acc[nb][1] + bias));
;           w.y = cvt_pk_bf16(gelu_tanh(bflo(uv.y)) * (acc[nb][2] + bias), gelu_tanh(bfhi(uv.y)) * (acc[nb][3] + bias));
;           *(u32x2*)(CAT + (size_t)(row0 + pp) * DM + h * 128 + c) = w; } }
	v_lshlrev_b32_e32 v26, 16, v124
	v_and_b32_e32 v27, 0xffff0000, v124
	v_mul_f32_e32 v28, 0x3dd2d3e8, v26
	v_mul_f32_e32 v29, 0x3dd2d3e8, v27
	v_fma_f32 v28, -v28, v26, s33
	v_fma_f32 v29, -v29, v27, s33
	v_mul_f32_e32 v28, v28, v26
	v_mul_f32_e32 v29, v29, v27
	v_exp_f32_e32 v28, v28
	v_exp_f32_e32 v29, v29
	v_add_f32_e32 v28, 1.0, v28
	v_add_f32_e32 v29, 1.0, v29
	v_rcp_f32_e32 v28, v28
	v_rcp_f32_e32 v29, v29
	s_nop 0
	v_pk_mul_f32 v[26:27], v[28:29], v[26:27]
	s_nop 0
	v_pk_mul_f32 v[22:23], v[22:23], v[26:27]
	v_lshlrev_b32_e32 v26, 16, v125
	v_cvt_pk_bf16_f32 v22, v22, v23
	v_mul_f32_e32 v23, 0x3dd2d3e8, v26
	v_fma_f32 v23, -v23, v26, s33
	v_mul_f32_e32 v23, v23, v26
	v_exp_f32_e32 v23, v23
	v_and_b32_e32 v27, 0xffff0000, v125
	v_add_f32_e32 v23, 1.0, v23
	v_rcp_f32_e32 v28, v23
	v_mul_f32_e32 v23, 0x3dd2d3e8, v27
	v_fma_f32 v23, -v23, v27, s33
	v_mul_f32_e32 v23, v23, v27
	v_exp_f32_e32 v23, v23
	s_nop 0
	v_add_f32_e32 v23, 1.0, v23
	v_rcp_f32_e32 v29, v23
	s_nop 0
	v_pk_mul_f32 v[26:27], v[28:29], v[26:27]
	s_nop 0
	v_pk_mul_f32 v[24:25], v[24:25], v[26:27]
	s_nop 0
	v_cvt_pk_bf16_f32 v23, v24, v25
	global_store_dwordx2 v[30:31], v[22:23], off offset:64
	s_waitcnt vmcnt(7)
	v_lshlrev_b32_e32 v22, 16, v126
	v_and_b32_e32 v23, 0xffff0000, v126
	v_mul_f32_e32 v24, 0x3dd2d3e8, v22
	v_mul_f32_e32 v25, 0x3dd2d3e8, v23
	v_fma_f32 v24, -v24, v22, s33
	v_fma_f32 v25, -v25, v23, s33
	v_mul_f32_e32 v24, v24, v22
	v_mul_f32_e32 v25, v25, v23
	v_exp_f32_e32 v24, v24
	v_exp_f32_e32 v25, v25
	v_add_f32_e32 v24, 1.0, v24
	v_add_f32_e32 v25, 1.0, v25
	v_rcp_f32_e32 v24, v24
	v_rcp_f32_e32 v25, v25
	s_nop 0
	v_pk_mul_f32 v[22:23], v[24:25], v[22:23]
	s_nop 0
	v_pk_mul_f32 v[18:19], v[18:19], v[22:23]
	v_lshlrev_b32_e32 v22, 16, v127
	v_cvt_pk_bf16_f32 v18, v18, v19
	v_mul_f32_e32 v19, 0x3dd2d3e8, v22
	v_fma_f32 v19, -v19, v22, s33
	v_mul_f32_e32 v19, v19, v22
	v_exp_f32_e32 v19, v19
	v_and_b32_e32 v23, 0xffff0000, v127
	v_add_f32_e32 v19, 1.0, v19
	v_rcp_f32_e32 v24, v19
	v_mul_f32_e32 v19, 0x3dd2d3e8, v23
	v_fma_f32 v19, -v19, v23, s33
	v_mul_f32_e32 v19, v19, v23
	v_exp_f32_e32 v19, v19
	s_nop 0
	v_add_f32_e32 v19, 1.0, v19
	v_rcp_f32_e32 v25, v19
	s_nop 0
	v_pk_mul_f32 v[22:23], v[24:25], v[22:23]
	s_nop 0
	v_pk_mul_f32 v[20:21], v[20:21], v[22:23]
	s_nop 0
	v_cvt_pk_bf16_f32 v19, v20, v21
	global_store_dwordx2 v[30:31], v[18:19], off offset:96
	s_waitcnt vmcnt(7)
	v_lshlrev_b32_e32 v18, 16, v128
	v_and_b32_e32 v19, 0xffff0000, v128
	v_mul_f32_e32 v20, 0x3dd2d3e8, v18
	v_mul_f32_e32 v21, 0x3dd2d3e8, v19
	v_fma_f32 v20, -v20, v18, s33
	v_fma_f32 v21, -v21, v19, s33
	v_mul_f32_e32 v20, v20, v18
	v_mul_f32_e32 v21, v21, v19
	v_exp_f32_e32 v20, v20
	v_exp_f32_e32 v21, v21
	v_add_f32_e32 v20, 1.0, v20
	v_add_f32_e32 v21, 1.0, v21
	v_rcp_f32_e32 v20, v20
	v_rcp_f32_e32 v21, v21
	s_nop 0
	v_pk_mul_f32 v[18:19], v[20:21], v[18:19]
	s_nop 0
	v_pk_mul_f32 v[14:15], v[14:15], v[18:19]
	v_lshlrev_b32_e32 v18, 16, v129
	v_cvt_pk_bf16_f32 v14, v14, v15
	v_mul_f32_e32 v15, 0x3dd2d3e8, v18
	v_fma_f32 v15, -v15, v18, s33
	v_mul_f32_e32 v15, v15, v18
	v_exp_f32_e32 v15, v15
	v_and_b32_e32 v19, 0xffff0000, v129
	v_add_f32_e32 v15, 1.0, v15
	v_rcp_f32_e32 v20, v15
	v_mul_f32_e32 v15, 0x3dd2d3e8, v19
	v_fma_f32 v15, -v15, v19, s33
	v_mul_f32_e32 v15, v15, v19
	v_exp_f32_e32 v15, v15
	s_nop 0
	v_add_f32_e32 v15, 1.0, v15
	v_rcp_f32_e32 v21, v15
	s_nop 0
	v_pk_mul_f32 v[18:19], v[20:21], v[18:19]
	s_nop 0
	v_pk_mul_f32 v[16:17], v[16:17], v[18:19]
	s_nop 0
	v_cvt_pk_bf16_f32 v15, v16, v17
	global_store_dwordx2 v[30:31], v[14:15], off offset:128
	s_waitcnt vmcnt(7)
; __device__ __forceinline__ unsigned cvt_pk_bf16(float lo, float hi) { const f32x2 v = {lo, hi}; const bf16x2_t b = __builtin_convertvector(v, bf16x2_t); return __builtin_bit_cast(unsigned, b); }
; __device__ __forceinline__ float bflo(unsigned w) { return __uint_as_float(w << 16); }
; __device__ __forceinline__ float bfhi(unsigned w) { return __uint_as_float(w & 0xffff0000u); }
; __device__ __forceinline__ void sgu_unit(const Params& p, int l, int un, LAS unsigned char* lds) {
;     ...
;       for (int nb = 0; nb < 8; ++nb) { const int c = nb * 16 + 4 * fq; const u32x2 uv = uq[nb];
;           u32x2 w; w.x = cvt_pk_bf16(gelu_tanh(bflo(uv.x)) * (acc[nb][0] + bias), gelu_tanh(bfhi(uv.x)) * (acc[nb][1] + bias));
;           w.y = cvt_pk_bf16(gelu_tanh(bflo(uv.y)) * (acc[nb][2] + bias), gelu_tanh(bfhi(uv.y)) * (acc[nb][3] + bias));
;           *(u32x2*)(CAT + (size_t)(row0 + pp) * DM + h * 128 + c) = w; } }
	v_lshlrev_b32_e32 v14, 16, v130
	v_and_b32_e32 v15, 0xffff0000, v130
	v_mul_f32_e32 v16, 0x3dd2d3e8, v14
	v_mul_f32_e32 v17, 0x3dd2d3e8, v15
	v_fma_f32 v16, -v16, v14, s33
	v_fma_f32 v17, -v17, v15, s33
	v_mul_f32_e32 v16, v16, v14
	v_mul_f32_e32 v17, v17, v15
	v_exp_f32_e32 v16, v16
	v_exp_f32_e32 v17, v17
	v_add_f32_e32 v16, 1.0, v16
	v_add_f32_e32 v17, 1.0, v17
	v_rcp_f32_e32 v16, v16
	v_rcp_f32_e32 v17, v17
	s_nop 0
	v_pk_mul_f32 v[14:15], v[16:17], v[14:15]
	s_nop 0
	v_pk_mul_f32 v[10:11], v[10:11], v[14:15]
	v_lshlrev_b32_e32 v14, 16, v131
	v_cvt_pk_bf16_f32 v10, v10, v11
	v_mul_f32_e32 v11, 0x3dd2d3e8, v14
	v_fma_f32 v11, -v11, v14, s33
	v_mul_f32_e32 v11, v11, v14
	v_exp_f32_e32 v11, v11
	v_and_b32_e32 v15, 0xffff0000, v131
	v_add_f32_e32 v11, 1.0, v11
	v_rcp_f32_e32 v16, v11
	v_mul_f32_e32 v11, 0x3dd2d3e8, v15
	v_fma_f32 v11, -v11, v15, s33
	v_mul_f32_e32 v11, v11, v15
	v_exp_f32_e32 v11, v11
	s_nop 0
	v_add_f32_e32 v11, 1.0, v11
	v_rcp_f32_e32 v17, v11
	s_nop 0
	v_pk_mul_f32 v[14:15], v[16:17], v[14:15]
	s_nop 0
	v_pk_mul_f32 v[12:13], v[12:13], v[14:15]
	s_nop 0
	v_cvt_pk_bf16_f32 v11, v12, v13
	global_store_dwordx2 v[30:31], v[10:11], off offset:160
	s_waitcnt vmcnt(7)
	v_lshlrev_b32_e32 v10, 16, v132
	v_and_b32_e32 v11, 0xffff0000, v132
	v_mul_f32_e32 v12, 0x3dd2d3e8, v10
	v_mul_f32_e32 v13, 0x3dd2d3e8, v11
	v_fma_f32 v12, -v12, v10, s33
	v_fma_f32 v13, -v13, v11, s33
	v_mul_f32_e32 v12, v12, v10
	v_mul_f32_e32 v13, v13, v11
	v_exp_f32_e32 v12, v12
	v_exp_f32_e32 v13, v13
	v_add_f32_e32 v12, 1.0, v12
	v_add_f32_e32 v13, 1.0, v13
	v_rcp_f32_e32 v12, v12
	v_rcp_f32_e32 v13, v13
	s_nop 0
	v_pk_mul_f32 v[10:11], v[12:13], v[10:11]
	s_nop 0
	v_pk_mul_f32 v[6:7], v[6:7], v[10:11]
	v_lshlrev_b32_e32 v10, 16, v133
	v_cvt_pk_bf16_f32 v6, v6, v7
	v_mul_f32_e32 v7, 0x3dd2d3e8, v10
	v_fma_f32 v7, -v7, v10, s33
	v_mul_f32_e32 v7, v7, v10
	v_exp_f32_e32 v7, v7
	v_and_b32_e32 v11, 0xffff0000, v133
	v_add_f32_e32 v7, 1.0, v7
	v_rcp_f32_e32 v12, v7
	v_mul_f32_e32 v7, 0x3dd2d3e8, v11
	v_fma_f32 v7, -v7, v11, s33
	v_mul_f32_e32 v7, v7, v11
	v_exp_f32_e32 v7, v7
	s_nop 0
	v_add_f32_e32 v7, 1.0, v7
	v_rcp_f32_e32 v13, v7
	s_nop 0
	v_pk_mul_f32 v[10:11], v[12:13], v[10:11]
	s_nop 0
	v_pk_mul_f32 v[8:9], v[8:9], v[10:11]
	s_nop 0
	v_cvt_pk_bf16_f32 v7, v8, v9
	global_store_dwordx2 v[30:31], v[6:7], off offset:192
	s_waitcnt vmcnt(7)
	v_lshlrev_b32_e32 v6, 16, v134
	v_and_b32_e32 v7, 0xffff0000, v134
	v_mul_f32_e32 v8, 0x3dd2d3e8, v6
	v_mul_f32_e32 v9, 0x3dd2d3e8, v7
	v_fma_f32 v8, -v8, v6, s33
	v_fma_f32 v9, -v9, v7, s33
	v_mul_f32_e32 v8, v8, v6
	v_mul_f32_e32 v9, v9, v7
	v_exp_f32_e32 v8, v8
	v_exp_f32_e32 v9, v9
	v_add_f32_e32 v8, 1.0, v8
	v_add_f32_e32 v9, 1.0, v9
	v_rcp_f32_e32 v8, v8
	v_rcp_f32_e32 v9, v9
	s_nop 0
	v_pk_mul_f32 v[6:7], v[8:9], v[6:7]
	s_nop 0
	v_pk_mul_f32 v[2:3], v[2:3], v[6:7]
	v_lshlrev_b32_e32 v6, 16, v135
	v_cvt_pk_bf16_f32 v2, v2, v3
	v_mul_f32_e32 v3, 0x3dd2d3e8, v6
	v_fma_f32 v3, -v3, v6, s33
	v_mul_f32_e32 v3, v3, v6
	v_exp_f32_e32 v3, v3
	v_and_b32_e32 v7, 0xffff0000, v135
	v_add_f32_e32 v3, 1.0, v3
	v_rcp_f32_e32 v8, v3
	v_mul_f32_e32 v3, 0x3dd2d3e8, v7
	v_fma_f32 v3, -v3, v7, s33
	v_mul_f32_e32 v3, v3, v7
	v_exp_f32_e32 v3, v3
	s_nop 0
	v_add_f32_e32 v3, 1.0, v3
	v_rcp_f32_e32 v9, v3
	s_nop 0
	v_pk_mul_f32 v[6:7], v[8:9], v[6:7]
	s_nop 0
	v_pk_mul_f32 v[4:5], v[4:5], v[6:7]
	s_nop 0
	v_cvt_pk_bf16_f32 v3, v4, v5
	global_store_dwordx2 v[30:31], v[2:3], off offset:224
	s_barrier
